# baseline (speedup 1.0000x reference)
.LBB0_34:
	s_lshr_b32 s0, s2, 2
	s_and_b32 s0, s0, 0x3ffffffe
	s_and_b32 s1, s2, 1
	v_lshrrev_b32_e32 v143, 7, v0
	s_bfe_u32 s3, s2, 0x20001
	s_or_b32 s0, s0, s1
	v_lshl_or_b32 v133, s0, 1, v143
	s_mul_i32 s0, s3, 0xc0
	v_bfe_u32 v135, v0, 6, 1
	s_movk_i32 s1, 0x60
	v_mov_b32_e32 v2, s0
	v_lshrrev_b32_e32 v3, 2, v0
	v_mad_u32_u24 v2, v135, s1, v2
	v_and_b32_e32 v142, 8, v3
	v_or_b32_e32 v2, v2, v142
	v_lshl_add_u32 v130, v2, 7, v133
	v_mov_b32_e32 v131, 0
	v_lshlrev_b64 v[2:3], 9, v[130:131]
	v_mul_u32_u24_e32 v4, 0x60, v135
	s_waitcnt lgkmcnt(0)
	v_lshl_add_u64 v[2:3], s[4:5], 0, v[2:3]
	v_lshlrev_b32_e32 v130, 4, v1
	v_lshl_add_u64 v[136:137], v[2:3], 0, v[130:131]
	v_lshlrev_b32_e32 v130, 2, v4
	v_lshl_add_u64 v[2:3], s[6:7], 0, v[130:131]
	s_movk_i32 s2, 0x300
	v_mad_u64_u32 v[4:5], s[0:1], v11, s2, v[2:3]
	v_mad_u64_u32 v[2:3], s[0:1], v10, s2, v[2:3]
	s_mov_b32 s0, 0x10000
	s_nop 0
	v_add_co_u32_e32 v14, vcc, s0, v136
	s_mov_b32 s0, 0x20000
	s_nop 0
	v_addc_co_u32_e32 v15, vcc, 0, v137, vcc
	v_add_co_u32_e32 v32, vcc, s0, v136
	v_lshlrev_b32_e32 v130, 2, v142
	s_nop 0
	v_addc_co_u32_e32 v33, vcc, 0, v137, vcc
	s_mov_b32 s0, 0x30000
	v_lshl_add_u64 v[140:141], v[2:3], 0, v[130:131]
	v_add_co_u32_e32 v2, vcc, s0, v136
	s_mov_b32 s0, 0x40000
	s_nop 0
	v_addc_co_u32_e32 v3, vcc, 0, v137, vcc
	v_lshl_add_u64 v[138:139], v[4:5], 0, v[130:131]
	v_add_co_u32_e32 v4, vcc, s0, v136
	s_mov_b32 s0, 0x50000
	s_nop 0
	v_addc_co_u32_e32 v5, vcc, 0, v137, vcc
	v_add_co_u32_e32 v34, vcc, s0, v136
	global_load_dwordx4 v[16:19], v[2:3], off nt
	global_load_dwordx4 v[20:23], v[4:5], off nt
	s_nop 0
	global_load_dwordx4 v[2:5], v[140:141], off offset:16
	global_load_dwordx4 v[6:9], v[140:141], off
	global_load_dwordx4 v[10:13], v[138:139], off offset:16
	global_load_dwordx4 v[24:27], v[138:139], off
	v_addc_co_u32_e32 v35, vcc, 0, v137, vcc
	s_mov_b32 s0, 0x60000
	v_add_co_u32_e32 v36, vcc, s0, v136
	s_mov_b32 s0, 0x70000
	s_nop 0
	v_addc_co_u32_e32 v37, vcc, 0, v137, vcc
	global_load_dwordx4 v[28:31], v[34:35], off nt
	global_load_dwordx4 v[48:51], v[36:37], off nt
	v_add_co_u32_e32 v34, vcc, s0, v136
	s_mov_b32 s0, 0x100000
	s_nop 0
	v_addc_co_u32_e32 v35, vcc, 0, v137, vcc
	global_load_dwordx4 v[52:55], v[34:35], off nt
	global_load_dwordx4 v[56:59], v[14:15], off nt
	global_load_dwordx4 v[60:63], v[32:33], off nt
	global_load_dwordx4 v[144:147], v[136:137], off nt
	s_mov_b32 s2, 0xffff
	s_lshl_b32 s3, s3, 16
	s_or_b32 s4, s3, 0x4000
	s_or_b32 s5, s3, 0x8000
	s_or_b32 s6, s3, 0xc000
	s_waitcnt vmcnt(9)
	v_pk_mul_f32 v[2:3], v[2:3], v[132:133] op_sel_hi:[1,0]
	s_waitcnt vmcnt(8)
	v_pk_mul_f32 v[6:7], v[6:7], v[132:133] op_sel_hi:[1,0]
	v_pk_mul_f32 v[8:9], v[8:9], v[132:133] op_sel_hi:[1,0]
	v_pk_mul_f32 v[4:5], v[4:5], v[132:133] op_sel_hi:[1,0]
	s_waitcnt vmcnt(6)
	v_pk_mul_f32 v[14:15], v[24:25], v[134:135] op_sel_hi:[1,0]
	v_pk_mul_f32 v[32:33], v[26:27], v[134:135] op_sel_hi:[1,0]
	v_pk_mul_f32 v[10:11], v[10:11], v[134:135] op_sel_hi:[1,0]
	v_cvt_pk_f16_f32 v24, v6, v7
	v_pk_mul_f32 v[6:7], v[12:13], v[134:135] op_sel_hi:[1,0]
	v_cvt_pk_f16_f32 v25, v8, v9
	v_cvt_pk_f16_f32 v26, v2, v3
	v_cvt_pk_f16_f32 v27, v4, v5
	v_cvt_pk_f16_f32 v148, v14, v15
	v_cvt_pk_f16_f32 v149, v32, v33
	v_cvt_pk_f16_f32 v150, v10, v11
	v_cvt_pk_f16_f32 v151, v6, v7
	v_add_co_u32_e32 v2, vcc, s0, v136
	s_mov_b32 s0, 0x110000
	s_nop 0
	v_addc_co_u32_e32 v3, vcc, 0, v137, vcc
	global_load_dwordx4 v[152:155], v[2:3], off nt
	s_waitcnt vmcnt(4)
	v_cvt_pk_f16_f32 v5, v48, v52
	v_cvt_pk_f16_f32 v4, v20, v28
	s_waitcnt vmcnt(2)
	v_cvt_pk_f16_f32 v3, v60, v16
	s_waitcnt vmcnt(1)
	v_cvt_pk_f16_f32 v2, v144, v56
	v_cvt_pk_f16_f32 v84, v22, v30
	v_add_co_u32_e32 v22, vcc, s0, v136
	v_mfma_f32_32x32x16_f16 v[98:113], v[24:27], v[2:5], 0
	v_cvt_pk_f16_f32 v85, v50, v54
	v_cvt_pk_f16_f32 v83, v62, v18
	v_cvt_pk_f16_f32 v82, v146, v58
	v_cvt_pk_f16_f32 v20, v23, v31
	v_cvt_pk_f16_f32 v19, v63, v19
	v_cvt_pk_f16_f32 v18, v147, v59
	v_addc_co_u32_e32 v23, vcc, 0, v137, vcc
	v_mfma_f32_32x32x16_f16 v[66:81], v[148:151], v[2:5], 0
	v_cvt_pk_f16_f32 v5, v49, v53
	v_cvt_pk_f16_f32 v4, v21, v29
	v_cvt_pk_f16_f32 v3, v61, v17
	v_cvt_pk_f16_f32 v2, v145, v57
	v_cvt_pk_f16_f32 v21, v51, v55
	s_mov_b32 s0, 0x120000
	global_load_dwordx4 v[144:147], v[140:141], off offset:80
	global_load_dwordx4 v[156:159], v[140:141], off offset:64
	v_mfma_f32_32x32x16_f16 v[34:49], v[24:27], v[2:5], 0
	global_load_dwordx4 v[160:163], v[138:139], off offset:80
	global_load_dwordx4 v[164:167], v[138:139], off offset:64
	s_waitcnt vmcnt(3)
	v_mul_f32_e64 v144, v144, v132
	v_mul_f32_e64 v145, v145, v132
	v_mfma_f32_32x32x16_f16 v[114:129], v[24:27], v[82:85], 0
	v_mfma_f32_32x32x16_f16 v[50:65], v[24:27], v[18:21], 0
	v_add_co_u32_e32 v24, vcc, s0, v136
	s_mov_b32 s0, 0x130000
	s_nop 0
	v_addc_co_u32_e32 v25, vcc, 0, v137, vcc
	v_add_co_u32_e32 v26, vcc, s0, v136
	s_mov_b32 s0, 0x140000
	s_nop 0
	v_addc_co_u32_e32 v27, vcc, 0, v137, vcc
	v_add_co_u32_e32 v28, vcc, s0, v136
	s_mov_b32 s0, 0x150000
	s_nop 0
	v_addc_co_u32_e32 v29, vcc, 0, v137, vcc
	v_add_co_u32_e32 v30, vcc, s0, v136
	s_mov_b32 s0, 0x160000
	s_nop 0
	v_addc_co_u32_e32 v31, vcc, 0, v137, vcc
	v_add_co_u32_e32 v32, vcc, s0, v136
	s_mov_b32 s0, 0x170000
	s_nop 0
	v_addc_co_u32_e32 v33, vcc, 0, v137, vcc
	global_load_dwordx4 v[168:171], v[30:31], off nt
	global_load_dwordx4 v[172:175], v[32:33], off nt
	v_add_co_u32_e32 v30, vcc, s0, v136
	v_mfma_f32_32x32x16_f16 v[2:17], v[148:151], v[2:5], 0
	s_nop 0
	v_addc_co_u32_e32 v31, vcc, 0, v137, vcc
	global_load_dwordx4 v[176:179], v[30:31], off nt
	global_load_dwordx4 v[180:183], v[26:27], off nt
	global_load_dwordx4 v[184:187], v[28:29], off nt
	global_load_dwordx4 v[188:191], v[24:25], off nt
	global_load_dwordx4 v[192:195], v[22:23], off nt
	s_mov_b32 s0, 0x200000
	v_mfma_f32_32x32x16_f16 v[82:97], v[148:151], v[82:85], 0
	v_mfma_f32_32x32x16_f16 v[18:33], v[148:151], v[18:21], 0
	s_waitcnt vmcnt(9)
	v_mul_f32_e64 v148, v156, v132
	v_mul_f32_e64 v149, v157, v132
	v_mul_f32_e64 v150, v158, v132
	v_mul_f32_e64 v151, v159, v132
	v_cvt_pk_f16_f32 v148, v148, v149
	v_cvt_pk_f16_f32 v149, v150, v151
	v_cvt_pk_f16_f32 v150, v144, v145
	v_pk_mul_f32 v[144:145], v[146:147], v[132:133] op_sel_hi:[1,0]
	s_waitcnt vmcnt(7)
	v_pk_mul_f32 v[146:147], v[166:167], v[134:135] op_sel_hi:[1,0]
	v_cvt_pk_f16_f32 v151, v144, v145
	v_pk_mul_f32 v[144:145], v[164:165], v[134:135] op_sel_hi:[1,0]
	v_add_co_u32_e32 v156, vcc, s0, v136
	v_cvt_pk_f16_f32 v144, v144, v145
	v_cvt_pk_f16_f32 v145, v146, v147
	v_pk_mul_f32 v[146:147], v[160:161], v[134:135] op_sel_hi:[1,0]
	v_pk_mul_f32 v[160:161], v[162:163], v[134:135] op_sel_hi:[1,0]
	v_addc_co_u32_e32 v157, vcc, 0, v137, vcc
	v_cvt_pk_f16_f32 v146, v146, v147
	v_cvt_pk_f16_f32 v147, v160, v161
	s_mov_b32 s0, 0x210000
	v_add_co_u32_e32 v196, vcc, s0, v136
	s_mov_b32 s0, 0x220000
	s_nop 0
	v_addc_co_u32_e32 v197, vcc, 0, v137, vcc
	global_load_dwordx4 v[156:159], v[156:157], off nt
	s_waitcnt vmcnt(5)
	v_cvt_pk_f16_f32 v163, v173, v177
	v_cvt_pk_f16_f32 v167, v172, v176
	s_waitcnt vmcnt(3)
	v_cvt_pk_f16_f32 v162, v185, v169
	s_waitcnt vmcnt(2)
	v_cvt_pk_f16_f32 v161, v189, v181
	s_waitcnt vmcnt(1)
	v_cvt_pk_f16_f32 v164, v152, v192
	v_add_co_u32_e32 v192, vcc, s0, v136
	v_cvt_pk_f16_f32 v160, v153, v193
	s_nop 0
	v_addc_co_u32_e32 v193, vcc, 0, v137, vcc
	s_mov_b32 s0, 0x230000
	v_cvt_pk_f16_f32 v166, v184, v168
	v_mfma_f32_32x32x16_f16 v[34:49], v[148:151], v[160:163], v[34:49]
	v_add_co_u32_e32 v184, vcc, s0, v136
	v_cvt_pk_f16_f32 v165, v188, v180
	s_nop 0
	v_addc_co_u32_e32 v185, vcc, 0, v137, vcc
	s_mov_b32 s0, 0x240000
	v_add_co_u32_e32 v188, vcc, s0, v136
	v_mfma_f32_32x32x16_f16 v[2:17], v[144:147], v[160:163], v[2:17]
	v_cvt_pk_f16_f32 v163, v174, v178
	v_cvt_pk_f16_f32 v162, v186, v170
	v_cvt_pk_f16_f32 v161, v190, v182
	v_cvt_pk_f16_f32 v160, v154, v194
	v_addc_co_u32_e32 v189, vcc, 0, v137, vcc
	s_mov_b32 s0, 0x250000
	v_mfma_f32_32x32x16_f16 v[114:129], v[148:151], v[160:163], v[114:129]
	v_add_co_u32_e32 v172, vcc, s0, v136
	s_mov_b32 s0, 0x260000
	s_nop 0
	v_addc_co_u32_e32 v173, vcc, 0, v137, vcc
	v_add_co_u32_e32 v176, vcc, s0, v136
	v_mfma_f32_32x32x16_f16 v[82:97], v[144:147], v[160:163], v[82:97]
	v_cvt_pk_f16_f32 v163, v175, v179
	v_cvt_pk_f16_f32 v162, v187, v171
	v_cvt_pk_f16_f32 v161, v191, v183
	v_cvt_pk_f16_f32 v160, v155, v195
	v_addc_co_u32_e32 v177, vcc, 0, v137, vcc
	s_mov_b32 s0, 0x270000
	v_mfma_f32_32x32x16_f16 v[98:113], v[148:151], v[164:167], v[98:113]
	v_add_co_u32_e32 v180, vcc, s0, v136
	s_mov_b32 s0, 0x300000
	s_nop 0
	v_addc_co_u32_e32 v181, vcc, 0, v137, vcc
	v_mfma_f32_32x32x16_f16 v[50:65], v[148:151], v[160:163], v[50:65]
	global_load_dwordx4 v[148:151], v[140:141], off offset:144
	global_load_dwordx4 v[152:155], v[140:141], off offset:128
	v_mfma_f32_32x32x16_f16 v[66:81], v[144:147], v[164:167], v[66:81]
	global_load_dwordx4 v[164:167], v[138:139], off offset:144
	global_load_dwordx4 v[168:171], v[138:139], off offset:128
	s_nop 0
	global_load_dwordx4 v[172:175], v[172:173], off nt
	s_nop 0
	global_load_dwordx4 v[176:179], v[176:177], off nt
	s_nop 0
	global_load_dwordx4 v[180:183], v[180:181], off nt
	s_nop 0
	global_load_dwordx4 v[184:187], v[184:185], off nt
	s_nop 0
	global_load_dwordx4 v[188:191], v[188:189], off nt
	s_nop 0
	global_load_dwordx4 v[192:195], v[192:193], off nt
	s_nop 0
	global_load_dwordx4 v[196:199], v[196:197], off nt
	v_mfma_f32_32x32x16_f16 v[18:33], v[144:147], v[160:163], v[18:33]
	s_waitcnt vmcnt(9)
	v_mul_f32_e64 v144, v152, v132
	v_mul_f32_e64 v145, v153, v132
	v_mul_f32_e64 v146, v154, v132
	v_mul_f32_e64 v147, v155, v132
	v_cvt_pk_f16_f32 v144, v144, v145
	v_cvt_pk_f16_f32 v145, v146, v147
	v_pk_mul_f32 v[146:147], v[148:149], v[132:133] op_sel_hi:[1,0]
	v_pk_mul_f32 v[148:149], v[150:151], v[132:133] op_sel_hi:[1,0]
	v_cvt_pk_f16_f32 v146, v146, v147
	v_cvt_pk_f16_f32 v147, v148, v149
	s_waitcnt vmcnt(7)
	v_pk_mul_f32 v[148:149], v[168:169], v[134:135] op_sel_hi:[1,0]
	v_pk_mul_f32 v[150:151], v[170:171], v[134:135] op_sel_hi:[1,0]
	v_cvt_pk_f16_f32 v148, v148, v149
	v_cvt_pk_f16_f32 v149, v150, v151
	v_pk_mul_f32 v[150:151], v[164:165], v[134:135] op_sel_hi:[1,0]
	v_pk_mul_f32 v[164:165], v[166:167], v[134:135] op_sel_hi:[1,0]
	v_cvt_pk_f16_f32 v150, v150, v151
	v_cvt_pk_f16_f32 v151, v164, v165
	v_add_co_u32_e32 v152, vcc, s0, v136
	s_mov_b32 s0, 0x310000
	s_nop 0
	v_addc_co_u32_e32 v153, vcc, 0, v137, vcc
	s_waitcnt vmcnt(4)
	v_cvt_pk_f16_f32 v163, v176, v180
	s_waitcnt vmcnt(2)
	v_cvt_pk_f16_f32 v162, v188, v172
	s_waitcnt vmcnt(1)
	v_cvt_pk_f16_f32 v161, v192, v184
	s_waitcnt vmcnt(0)
	v_cvt_pk_f16_f32 v160, v156, v196
	v_add_co_u32_e32 v196, vcc, s0, v136
	s_nop 0
	v_mfma_f32_32x32x16_f16 v[98:113], v[144:147], v[160:163], v[98:113]
	s_mov_b32 s0, 0x320000
	global_load_dwordx4 v[152:155], v[152:153], off nt
	v_mfma_f32_32x32x16_f16 v[66:81], v[148:151], v[160:163], v[66:81]
	v_cvt_pk_f16_f32 v160, v157, v197
	v_addc_co_u32_e32 v197, vcc, 0, v137, vcc
	v_add_co_u32_e32 v192, vcc, s0, v136
	v_cvt_pk_f16_f32 v163, v177, v181
	v_cvt_pk_f16_f32 v162, v189, v173
	v_cvt_pk_f16_f32 v161, v193, v185
	v_addc_co_u32_e32 v193, vcc, 0, v137, vcc
	s_mov_b32 s0, 0x330000
	v_mfma_f32_32x32x16_f16 v[34:49], v[144:147], v[160:163], v[34:49]
	v_add_co_u32_e32 v184, vcc, s0, v136
	s_mov_b32 s0, 0x340000
	s_nop 0
	v_addc_co_u32_e32 v185, vcc, 0, v137, vcc
	v_add_co_u32_e32 v188, vcc, s0, v136
	v_mfma_f32_32x32x16_f16 v[2:17], v[148:151], v[160:163], v[2:17]
	v_cvt_pk_f16_f32 v163, v178, v182
	v_cvt_pk_f16_f32 v162, v190, v174
	v_cvt_pk_f16_f32 v161, v194, v186
	v_cvt_pk_f16_f32 v160, v158, v198
	v_addc_co_u32_e32 v189, vcc, 0, v137, vcc
	s_mov_b32 s0, 0x350000
	v_mfma_f32_32x32x16_f16 v[114:129], v[144:147], v[160:163], v[114:129]
	v_add_co_u32_e32 v172, vcc, s0, v136
	s_mov_b32 s0, 0x360000
	s_nop 0
	v_addc_co_u32_e32 v173, vcc, 0, v137, vcc
	v_add_co_u32_e32 v176, vcc, s0, v136
	v_mfma_f32_32x32x16_f16 v[82:97], v[148:151], v[160:163], v[82:97]
	v_cvt_pk_f16_f32 v163, v179, v183
	v_cvt_pk_f16_f32 v162, v191, v175
	v_cvt_pk_f16_f32 v161, v195, v187
	v_cvt_pk_f16_f32 v160, v159, v199
	v_addc_co_u32_e32 v177, vcc, 0, v137, vcc
	s_mov_b32 s0, 0x370000
	v_mfma_f32_32x32x16_f16 v[50:65], v[144:147], v[160:163], v[50:65]
	global_load_dwordx4 v[144:147], v[140:141], off offset:208
	global_load_dwordx4 v[156:159], v[140:141], off offset:192
	global_load_dwordx4 v[164:167], v[138:139], off offset:208
	global_load_dwordx4 v[168:171], v[138:139], off offset:192
	v_add_co_u32_e32 v180, vcc, s0, v136
	global_load_dwordx4 v[172:175], v[172:173], off nt
	s_nop 0
	global_load_dwordx4 v[176:179], v[176:177], off nt
	v_addc_co_u32_e32 v181, vcc, 0, v137, vcc
	global_load_dwordx4 v[180:183], v[180:181], off nt
	s_nop 0
	global_load_dwordx4 v[184:187], v[184:185], off nt
	s_nop 0
	global_load_dwordx4 v[188:191], v[188:189], off nt
	s_nop 0
	global_load_dwordx4 v[192:195], v[192:193], off nt
	s_nop 0
	global_load_dwordx4 v[196:199], v[196:197], off nt
	v_mfma_f32_32x32x16_f16 v[18:33], v[148:151], v[160:163], v[18:33]
	s_mov_b32 s0, 0x400000
	s_waitcnt vmcnt(10)
	v_mul_f32_e64 v144, v144, v132
	v_mul_f32_e64 v145, v145, v132
	s_waitcnt vmcnt(9)
	v_pk_mul_f32 v[148:149], v[156:157], v[132:133] op_sel_hi:[1,0]
	v_pk_mul_f32 v[150:151], v[158:159], v[132:133] op_sel_hi:[1,0]
	v_cvt_pk_f16_f32 v148, v148, v149
	v_cvt_pk_f16_f32 v149, v150, v151
	v_cvt_pk_f16_f32 v150, v144, v145
	v_pk_mul_f32 v[144:145], v[146:147], v[132:133] op_sel_hi:[1,0]
	s_waitcnt vmcnt(7)
	v_pk_mul_f32 v[146:147], v[170:171], v[134:135] op_sel_hi:[1,0]
	v_cvt_pk_f16_f32 v151, v144, v145
	v_pk_mul_f32 v[144:145], v[168:169], v[134:135] op_sel_hi:[1,0]
	v_add_co_u32_e32 v156, vcc, s0, v136
	v_cvt_pk_f16_f32 v144, v144, v145
	v_cvt_pk_f16_f32 v145, v146, v147
	v_pk_mul_f32 v[146:147], v[164:165], v[134:135] op_sel_hi:[1,0]
	v_pk_mul_f32 v[164:165], v[166:167], v[134:135] op_sel_hi:[1,0]
	v_cvt_pk_f16_f32 v146, v146, v147
	v_cvt_pk_f16_f32 v147, v164, v165
	v_addc_co_u32_e32 v157, vcc, 0, v137, vcc
	s_mov_b32 s0, 0x410000
	s_waitcnt vmcnt(4)
	v_cvt_pk_f16_f32 v163, v176, v180
	s_waitcnt vmcnt(2)
	v_cvt_pk_f16_f32 v162, v188, v172
	s_waitcnt vmcnt(1)
	v_cvt_pk_f16_f32 v161, v192, v184
	s_waitcnt vmcnt(0)
	v_cvt_pk_f16_f32 v160, v152, v196
	v_add_co_u32_e32 v196, vcc, s0, v136
	s_nop 0
	v_mfma_f32_32x32x16_f16 v[98:113], v[148:151], v[160:163], v[98:113]
	s_mov_b32 s0, 0x420000
	global_load_dwordx4 v[156:159], v[156:157], off nt
	v_mfma_f32_32x32x16_f16 v[66:81], v[144:147], v[160:163], v[66:81]
	v_cvt_pk_f16_f32 v160, v153, v197
	v_addc_co_u32_e32 v197, vcc, 0, v137, vcc
	v_add_co_u32_e32 v192, vcc, s0, v136
	v_cvt_pk_f16_f32 v163, v177, v181
	v_cvt_pk_f16_f32 v162, v189, v173
	v_cvt_pk_f16_f32 v161, v193, v185
	v_addc_co_u32_e32 v193, vcc, 0, v137, vcc
	s_mov_b32 s0, 0x430000
	v_mfma_f32_32x32x16_f16 v[34:49], v[148:151], v[160:163], v[34:49]
	v_add_co_u32_e32 v184, vcc, s0, v136
	s_mov_b32 s0, 0x440000
	s_nop 0
	v_addc_co_u32_e32 v185, vcc, 0, v137, vcc
	v_add_co_u32_e32 v188, vcc, s0, v136
	v_mfma_f32_32x32x16_f16 v[2:17], v[144:147], v[160:163], v[2:17]
	v_cvt_pk_f16_f32 v163, v178, v182
	v_cvt_pk_f16_f32 v162, v190, v174
	v_cvt_pk_f16_f32 v161, v194, v186
	v_cvt_pk_f16_f32 v160, v154, v198
	v_addc_co_u32_e32 v189, vcc, 0, v137, vcc
	s_mov_b32 s0, 0x450000
	v_mfma_f32_32x32x16_f16 v[114:129], v[148:151], v[160:163], v[114:129]
	v_add_co_u32_e32 v172, vcc, s0, v136
	s_mov_b32 s0, 0x460000
	s_nop 0
	v_addc_co_u32_e32 v173, vcc, 0, v137, vcc
	v_add_co_u32_e32 v176, vcc, s0, v136
	v_mfma_f32_32x32x16_f16 v[82:97], v[144:147], v[160:163], v[82:97]
	v_cvt_pk_f16_f32 v163, v179, v183
	v_cvt_pk_f16_f32 v162, v191, v175
	v_cvt_pk_f16_f32 v161, v195, v187
	v_cvt_pk_f16_f32 v160, v155, v199
	v_addc_co_u32_e32 v177, vcc, 0, v137, vcc
	s_mov_b32 s0, 0x470000
	v_mfma_f32_32x32x16_f16 v[50:65], v[148:151], v[160:163], v[50:65]
	global_load_dwordx4 v[148:151], v[140:141], off offset:272
	global_load_dwordx4 v[152:155], v[140:141], off offset:256
	global_load_dwordx4 v[164:167], v[138:139], off offset:272
	global_load_dwordx4 v[168:171], v[138:139], off offset:256
	v_add_co_u32_e32 v180, vcc, s0, v136
	global_load_dwordx4 v[172:175], v[172:173], off nt
	s_nop 0
	global_load_dwordx4 v[176:179], v[176:177], off nt
	v_addc_co_u32_e32 v181, vcc, 0, v137, vcc
	global_load_dwordx4 v[180:183], v[180:181], off nt
	s_nop 0
	global_load_dwordx4 v[184:187], v[184:185], off nt
	s_nop 0
	global_load_dwordx4 v[188:191], v[188:189], off nt
	s_nop 0
	global_load_dwordx4 v[192:195], v[192:193], off nt
	s_nop 0
	global_load_dwordx4 v[196:199], v[196:197], off nt
	v_mfma_f32_32x32x16_f16 v[18:33], v[144:147], v[160:163], v[18:33]
	s_mov_b32 s0, 0x500000
	s_waitcnt vmcnt(9)
	v_mul_f32_e64 v144, v152, v132
	v_mul_f32_e64 v145, v153, v132
	v_mul_f32_e64 v146, v154, v132
	v_mul_f32_e64 v147, v155, v132
	v_cvt_pk_f16_f32 v144, v144, v145
	v_cvt_pk_f16_f32 v145, v146, v147
	v_pk_mul_f32 v[146:147], v[148:149], v[132:133] op_sel_hi:[1,0]
	v_pk_mul_f32 v[148:149], v[150:151], v[132:133] op_sel_hi:[1,0]
	v_cvt_pk_f16_f32 v146, v146, v147
	v_cvt_pk_f16_f32 v147, v148, v149
	s_waitcnt vmcnt(7)
	v_pk_mul_f32 v[148:149], v[168:169], v[134:135] op_sel_hi:[1,0]
	v_pk_mul_f32 v[150:151], v[170:171], v[134:135] op_sel_hi:[1,0]
	v_cvt_pk_f16_f32 v148, v148, v149
	v_cvt_pk_f16_f32 v149, v150, v151
	v_pk_mul_f32 v[150:151], v[164:165], v[134:135] op_sel_hi:[1,0]
	v_pk_mul_f32 v[164:165], v[166:167], v[134:135] op_sel_hi:[1,0]
	v_cvt_pk_f16_f32 v150, v150, v151
	v_cvt_pk_f16_f32 v151, v164, v165
	v_add_co_u32_e32 v152, vcc, s0, v136
	s_mov_b32 s0, 0x510000
	s_nop 0
	v_addc_co_u32_e32 v153, vcc, 0, v137, vcc
	s_waitcnt vmcnt(4)
	v_cvt_pk_f16_f32 v163, v176, v180
	s_waitcnt vmcnt(2)
	v_cvt_pk_f16_f32 v162, v188, v172
	s_waitcnt vmcnt(1)
	v_cvt_pk_f16_f32 v161, v192, v184
	s_waitcnt vmcnt(0)
	v_cvt_pk_f16_f32 v160, v156, v196
	v_add_co_u32_e32 v192, vcc, s0, v136
	s_nop 0
	v_mfma_f32_32x32x16_f16 v[98:113], v[144:147], v[160:163], v[98:113]
	s_mov_b32 s0, 0x520000
	global_load_dwordx4 v[152:155], v[152:153], off nt
	v_mfma_f32_32x32x16_f16 v[66:81], v[148:151], v[160:163], v[66:81]
	v_cvt_pk_f16_f32 v161, v193, v185
	v_addc_co_u32_e32 v193, vcc, 0, v137, vcc
	v_add_co_u32_e32 v188, vcc, s0, v136
	v_cvt_pk_f16_f32 v162, v189, v173
	s_nop 0
	v_addc_co_u32_e32 v189, vcc, 0, v137, vcc
	s_mov_b32 s0, 0x530000
	v_add_co_u32_e32 v180, vcc, s0, v136
	v_cvt_pk_f16_f32 v163, v177, v181
	v_cvt_pk_f16_f32 v160, v157, v197
	v_addc_co_u32_e32 v181, vcc, 0, v137, vcc
	s_mov_b32 s0, 0x540000
	v_mfma_f32_32x32x16_f16 v[34:49], v[144:147], v[160:163], v[34:49]
	v_add_co_u32_e32 v184, vcc, s0, v136
	s_mov_b32 s0, 0x550000
	s_nop 0
	v_addc_co_u32_e32 v185, vcc, 0, v137, vcc
	v_add_co_u32_e32 v164, vcc, s0, v136
	v_mfma_f32_32x32x16_f16 v[2:17], v[148:151], v[160:163], v[2:17]
	v_cvt_pk_f16_f32 v163, v178, v182
	v_cvt_pk_f16_f32 v162, v190, v174
	v_cvt_pk_f16_f32 v161, v194, v186
	v_cvt_pk_f16_f32 v160, v158, v198
	v_addc_co_u32_e32 v165, vcc, 0, v137, vcc
	s_mov_b32 s0, 0x560000
	v_mfma_f32_32x32x16_f16 v[114:129], v[144:147], v[160:163], v[114:129]
	v_mfma_f32_32x32x16_f16 v[82:97], v[148:151], v[160:163], v[82:97]
	v_cvt_pk_f16_f32 v163, v179, v183
	v_cvt_pk_f16_f32 v162, v191, v175
	v_cvt_pk_f16_f32 v161, v195, v187
	v_cvt_pk_f16_f32 v160, v159, v199
	s_nop 1
	v_mfma_f32_32x32x16_f16 v[50:65], v[144:147], v[160:163], v[50:65]
	global_load_dwordx4 v[144:147], v[140:141], off offset:336
	global_load_dwordx4 v[156:159], v[140:141], off offset:320
	v_add_co_u32_e32 v140, vcc, s0, v136
	s_mov_b32 s0, 0x570000
	s_nop 0
	v_addc_co_u32_e32 v141, vcc, 0, v137, vcc
	global_load_dwordx4 v[164:167], v[164:165], off nt
	s_nop 0
	global_load_dwordx4 v[168:171], v[140:141], off
	global_load_dwordx4 v[172:175], v[138:139], off offset:336
	s_nop 0
	global_load_dwordx4 v[138:141], v[138:139], off offset:320
	v_add_co_u32_e32 v136, vcc, s0, v136
	v_mfma_f32_32x32x16_f16 v[18:33], v[148:151], v[160:163], v[18:33]
	s_nop 0
	v_addc_co_u32_e32 v137, vcc, 0, v137, vcc
	global_load_dwordx4 v[176:179], v[136:137], off nt
	s_nop 0
	global_load_dwordx4 v[180:183], v[180:181], off nt
	s_nop 0
	global_load_dwordx4 v[184:187], v[184:185], off nt
	s_nop 0
	global_load_dwordx4 v[188:191], v[188:189], off nt
	s_nop 0
	global_load_dwordx4 v[192:195], v[192:193], off nt
	v_cmp_eq_u32_e32 vcc, 0, v135
	s_waitcnt vmcnt(9)
	v_pk_mul_f32 v[136:137], v[156:157], v[132:133] op_sel_hi:[1,0]
	s_nop 0
	v_cvt_pk_f16_f32 v148, v136, v137
	v_pk_mul_f32 v[136:137], v[158:159], v[132:133] op_sel_hi:[1,0]
	s_nop 0
	v_cvt_pk_f16_f32 v149, v136, v137
	v_pk_mul_f32 v[136:137], v[144:145], v[132:133] op_sel_hi:[1,0]
	s_waitcnt vmcnt(1)
	v_cvt_pk_f16_f32 v145, v188, v180
	v_cvt_pk_f16_f32 v150, v136, v137
	v_pk_mul_f32 v[136:137], v[146:147], v[132:133] op_sel_hi:[1,0]
	v_cvt_pk_f16_f32 v147, v168, v176
	v_cvt_pk_f16_f32 v151, v136, v137
	v_pk_mul_f32 v[136:137], v[138:139], v[134:135] op_sel_hi:[1,0]
	v_pk_mul_f32 v[138:139], v[140:141], v[134:135] op_sel_hi:[1,0]
	v_cvt_pk_f16_f32 v136, v136, v137
	v_cvt_pk_f16_f32 v137, v138, v139
	v_pk_mul_f32 v[138:139], v[172:173], v[134:135] op_sel_hi:[1,0]
	v_pk_mul_f32 v[140:141], v[174:175], v[134:135] op_sel_hi:[1,0]
	v_cvt_pk_f16_f32 v138, v138, v139
	v_cvt_pk_f16_f32 v139, v140, v141
	v_cvt_pk_f16_f32 v146, v184, v164
	s_waitcnt vmcnt(0)
	v_cvt_pk_f16_f32 v144, v152, v192
	v_and_b32_e32 v132, 63, v0
	v_lshlrev_b32_e32 v0, 2, v132
	v_mfma_f32_32x32x16_f16 v[98:113], v[148:151], v[144:147], v[98:113]
	v_lshl_or_b32 v140, v143, 15, v0
	v_lshlrev_b32_e32 v141, 14, v135
	v_or_b32_e32 v130, v140, v141
	v_mfma_f32_32x32x16_f16 v[66:81], v[136:139], v[144:147], v[66:81]
	v_cvt_pk_f16_f32 v147, v169, v177
	v_cvt_pk_f16_f32 v146, v185, v165
	v_cvt_pk_f16_f32 v145, v189, v181
	v_cvt_pk_f16_f32 v144, v153, v193
	s_nop 1
	v_mfma_f32_32x32x16_f16 v[34:49], v[148:151], v[144:147], v[34:49]
	v_mfma_f32_32x32x16_f16 v[2:17], v[136:139], v[144:147], v[2:17]
	v_cvt_pk_f16_f32 v147, v170, v178
	v_cvt_pk_f16_f32 v146, v186, v166
	v_cvt_pk_f16_f32 v145, v190, v182
	v_cvt_pk_f16_f32 v144, v154, v194
	s_nop 1
	v_mfma_f32_32x32x16_f16 v[114:129], v[148:151], v[144:147], v[114:129]
	v_mfma_f32_32x32x16_f16 v[82:97], v[136:139], v[144:147], v[82:97]
	s_nop 10
	v_cndmask_b32_e32 v0, v98, v114, vcc
	v_cndmask_b32_e32 v134, v99, v115, vcc
	ds_write2st64_b32 v130, v0, v134 offset1:1
	v_cndmask_b32_e32 v0, v100, v116, vcc
	v_cndmask_b32_e32 v134, v101, v117, vcc
	ds_write2st64_b32 v130, v0, v134 offset0:2 offset1:3
	v_cndmask_b32_e32 v0, v102, v118, vcc
	v_cndmask_b32_e32 v134, v103, v119, vcc
	ds_write2st64_b32 v130, v0, v134 offset0:4 offset1:5
	v_cndmask_b32_e32 v0, v104, v120, vcc
	v_cndmask_b32_e32 v134, v105, v121, vcc
	ds_write2st64_b32 v130, v0, v134 offset0:6 offset1:7
	v_cndmask_b32_e32 v0, v106, v122, vcc
	v_cndmask_b32_e32 v134, v107, v123, vcc
	ds_write2st64_b32 v130, v0, v134 offset0:8 offset1:9
	v_cndmask_b32_e32 v0, v108, v124, vcc
	v_cndmask_b32_e32 v134, v109, v125, vcc
	ds_write2st64_b32 v130, v0, v134 offset0:10 offset1:11
	v_cndmask_b32_e32 v0, v110, v126, vcc
	v_cndmask_b32_e32 v134, v111, v127, vcc
	v_cvt_pk_f16_f32 v147, v171, v179
	v_cvt_pk_f16_f32 v146, v187, v167
	v_cvt_pk_f16_f32 v145, v191, v183
	v_cvt_pk_f16_f32 v144, v155, v195
	ds_write2st64_b32 v130, v0, v134 offset0:12 offset1:13
	v_cndmask_b32_e32 v0, v112, v128, vcc
	v_cndmask_b32_e32 v134, v113, v129, vcc
	v_mfma_f32_32x32x16_f16 v[50:65], v[148:151], v[144:147], v[50:65]
	ds_write2st64_b32 v130, v0, v134 offset0:14 offset1:15
	v_cndmask_b32_e32 v0, v66, v82, vcc
	v_cndmask_b32_e32 v134, v67, v83, vcc
	ds_write2st64_b32 v130, v0, v134 offset0:16 offset1:17
	v_cndmask_b32_e32 v0, v68, v84, vcc
	v_cndmask_b32_e32 v134, v69, v85, vcc
	ds_write2st64_b32 v130, v0, v134 offset0:18 offset1:19
	v_cndmask_b32_e32 v0, v70, v86, vcc
	v_cndmask_b32_e32 v134, v71, v87, vcc
	ds_write2st64_b32 v130, v0, v134 offset0:20 offset1:21
	v_cndmask_b32_e32 v0, v72, v88, vcc
	v_cndmask_b32_e32 v134, v73, v89, vcc
	ds_write2st64_b32 v130, v0, v134 offset0:22 offset1:23
	v_cndmask_b32_e32 v0, v74, v90, vcc
	v_cndmask_b32_e32 v134, v75, v91, vcc
	ds_write2st64_b32 v130, v0, v134 offset0:24 offset1:25
	v_cndmask_b32_e32 v0, v76, v92, vcc
	v_cndmask_b32_e32 v134, v77, v93, vcc
	ds_write2st64_b32 v130, v0, v134 offset0:26 offset1:27
	v_cndmask_b32_e32 v0, v78, v94, vcc
	v_cndmask_b32_e32 v134, v79, v95, vcc
	ds_write2st64_b32 v130, v0, v134 offset0:28 offset1:29
	v_cndmask_b32_e32 v0, v80, v96, vcc
	v_cndmask_b32_e32 v134, v81, v97, vcc
	v_mfma_f32_32x32x16_f16 v[18:33], v[136:139], v[144:147], v[18:33]
	ds_write2st64_b32 v130, v0, v134 offset0:30 offset1:31
	v_cndmask_b32_e32 v0, v34, v50, vcc
	v_cndmask_b32_e32 v134, v35, v51, vcc
	ds_write2st64_b32 v130, v0, v134 offset0:32 offset1:33
	v_cndmask_b32_e32 v0, v36, v52, vcc
	v_cndmask_b32_e32 v134, v37, v53, vcc
	ds_write2st64_b32 v130, v0, v134 offset0:34 offset1:35
	v_cndmask_b32_e32 v0, v38, v54, vcc
	v_cndmask_b32_e32 v134, v39, v55, vcc
	ds_write2st64_b32 v130, v0, v134 offset0:36 offset1:37
	v_cndmask_b32_e32 v0, v40, v56, vcc
	v_cndmask_b32_e32 v134, v41, v57, vcc
	ds_write2st64_b32 v130, v0, v134 offset0:38 offset1:39
	v_cndmask_b32_e32 v0, v42, v58, vcc
	v_cndmask_b32_e32 v134, v43, v59, vcc
	ds_write2st64_b32 v130, v0, v134 offset0:40 offset1:41
	v_cndmask_b32_e32 v0, v44, v60, vcc
	v_cndmask_b32_e32 v134, v45, v61, vcc
	ds_write2st64_b32 v130, v0, v134 offset0:42 offset1:43
	v_cndmask_b32_e32 v0, v46, v62, vcc
	v_cndmask_b32_e32 v134, v47, v63, vcc
	ds_write2st64_b32 v130, v0, v134 offset0:44 offset1:45
	v_cndmask_b32_e32 v0, v48, v64, vcc
	v_cndmask_b32_e32 v134, v49, v65, vcc
	ds_write2st64_b32 v130, v0, v134 offset0:46 offset1:47
	v_cndmask_b32_e32 v0, v2, v18, vcc
	v_cndmask_b32_e32 v134, v3, v19, vcc
	ds_write2st64_b32 v130, v0, v134 offset0:48 offset1:49
	v_cndmask_b32_e32 v0, v4, v20, vcc
	v_cndmask_b32_e32 v134, v5, v21, vcc
	ds_write2st64_b32 v130, v0, v134 offset0:50 offset1:51
	v_cndmask_b32_e32 v0, v6, v22, vcc
	v_cndmask_b32_e32 v134, v7, v23, vcc
	ds_write2st64_b32 v130, v0, v134 offset0:52 offset1:53
	v_cndmask_b32_e32 v0, v8, v24, vcc
	v_cndmask_b32_e32 v134, v9, v25, vcc
	ds_write2st64_b32 v130, v0, v134 offset0:54 offset1:55
	v_cndmask_b32_e32 v0, v10, v26, vcc
	v_cndmask_b32_e32 v134, v11, v27, vcc
	ds_write2st64_b32 v130, v0, v134 offset0:56 offset1:57
	v_cndmask_b32_e32 v0, v12, v28, vcc
	v_cndmask_b32_e32 v134, v13, v29, vcc
	ds_write2st64_b32 v130, v0, v134 offset0:58 offset1:59
	v_cndmask_b32_e32 v0, v14, v30, vcc
	v_cndmask_b32_e32 v134, v15, v31, vcc
	ds_write2st64_b32 v130, v0, v134 offset0:60 offset1:61
	v_cndmask_b32_e32 v0, v16, v32, vcc
	v_cndmask_b32_e32 v134, v17, v33, vcc
	ds_write2st64_b32 v130, v0, v134 offset0:62 offset1:63
	v_lshlrev_b32_e32 v0, 2, v1
	v_lshl_or_b32 v143, v135, 1, v0
	v_mbcnt_lo_u32_b32 v0, -1, 0
	v_mbcnt_hi_u32_b32 v0, -1, v0
	v_and_b32_e32 v130, 64, v0
	v_xor_b32_e32 v1, 32, v0
	v_add_u32_e32 v130, 64, v130
	v_cmp_lt_i32_e64 s[0:1], v1, v130
	v_lshlrev_b32_e32 v130, 1, v142
	s_waitcnt lgkmcnt(0)
	v_cndmask_b32_e64 v0, v0, v1, s[0:1]
	v_lshlrev_b32_e32 v144, 2, v0
	v_xor_b32_e32 v0, 0x4000, v141
	v_or_b32_e32 v142, v140, v0
	s_barrier
	ds_read2st64_b32 v[0:1], v142 offset1:1
	ds_read2st64_b32 v[134:135], v142 offset0:4 offset1:5
	ds_read2st64_b32 v[136:137], v142 offset0:6 offset1:7
	ds_read2st64_b32 v[138:139], v142 offset0:2 offset1:3
	v_cndmask_b32_e32 v98, v114, v98, vcc
	v_cndmask_b32_e32 v102, v118, v102, vcc
	s_waitcnt lgkmcnt(3)
	v_add_f32_e32 v0, v98, v0
	s_waitcnt lgkmcnt(2)
	v_add_f32_e32 v98, v102, v134
	v_cndmask_b32_e32 v99, v115, v99, vcc
	v_cndmask_b32_e32 v102, v119, v103, vcc
	v_add_f32_e32 v1, v99, v1
	v_add_f32_e32 v99, v102, v135
	v_cndmask_b32_e32 v100, v116, v100, vcc
	v_cndmask_b32_e32 v102, v120, v104, vcc
	v_cndmask_b32_e32 v101, v117, v101, vcc
	v_cndmask_b32_e32 v103, v121, v105, vcc
	s_waitcnt lgkmcnt(0)
	v_add_f32_e32 v100, v100, v138
	v_add_f32_e32 v102, v102, v136
	v_add_f32_e32 v101, v101, v139
	v_cvt_pk_f16_f32 v104, v0, v1
	v_add_f32_e32 v0, v103, v137
	v_cvt_pk_f16_f32 v100, v100, v101
	v_cvt_pk_f16_f32 v101, v98, v99
	v_cvt_pk_f16_f32 v102, v102, v0
	v_cmp_gt_u32_e64 s[0:1], 32, v132
	v_mov_b32_e32 v120, 0x3c00
	v_bfrev_b32_e32 v121, 60
	v_cndmask_b32_e64 v0, v100, v102, s[0:1]
	v_cndmask_b32_e64 v1, v104, v101, s[0:1]
	ds_bpermute_b32 v103, v144, v0
	ds_bpermute_b32 v105, v144, v1
	v_cndmask_b32_e32 v106, v122, v106, vcc
	v_cndmask_b32_e32 v110, v126, v110, vcc
	v_lshlrev_b32_e32 v145, 7, v133
	s_waitcnt lgkmcnt(1)
	v_cndmask_b32_e64 v99, v103, v100, s[0:1]
	v_cndmask_b32_e64 v100, v102, v103, s[0:1]
	s_waitcnt lgkmcnt(0)
	v_cndmask_b32_e64 v102, v101, v105, s[0:1]
	v_cndmask_b32_e64 v103, v120, v102, s[0:1]
	v_cndmask_b32_e64 v101, v121, v100, s[0:1]
	v_cndmask_b32_e64 v98, v105, v104, s[0:1]
	v_bfi_b32 v101, s2, v100, v101
	v_bfi_b32 v100, s2, v103, v102
	ds_read2st64_b32 v[102:103], v142 offset0:8 offset1:9
	ds_read2st64_b32 v[104:105], v142 offset0:12 offset1:13
	ds_read2st64_b32 v[114:115], v142 offset0:14 offset1:15
	ds_read2st64_b32 v[116:117], v142 offset0:10 offset1:11
	v_or_b32_e32 v119, v143, v145
	v_lshl_add_u64 v[0:1], s[8:9], 0, v[130:131]
	s_waitcnt lgkmcnt(3)
	v_add_f32_e32 v102, v106, v102
	v_cndmask_b32_e32 v106, v123, v107, vcc
	v_cndmask_b32_e32 v107, v127, v111, vcc
	v_add_f32_e32 v103, v106, v103
	s_waitcnt lgkmcnt(2)
	v_add_f32_e32 v105, v107, v105
	v_cndmask_b32_e32 v106, v124, v108, vcc
	v_cndmask_b32_e32 v107, v128, v112, vcc
	v_cndmask_b32_e32 v108, v125, v109, vcc
	v_cndmask_b32_e32 v109, v129, v113, vcc
	v_add_f32_e32 v104, v110, v104
	s_waitcnt lgkmcnt(0)
	v_add_f32_e32 v106, v106, v116
	v_add_f32_e32 v107, v107, v114
	v_add_f32_e32 v108, v108, v117
	v_cvt_pk_f16_f32 v110, v102, v103
	v_add_f32_e32 v102, v109, v115
	v_cvt_pk_f16_f32 v106, v106, v108
	v_cvt_pk_f16_f32 v104, v104, v105
	v_cvt_pk_f16_f32 v105, v107, v102
	v_cndmask_b32_e64 v102, v106, v105, s[0:1]
	v_cndmask_b32_e64 v103, v110, v104, s[0:1]
	ds_bpermute_b32 v107, v144, v102
	ds_bpermute_b32 v108, v144, v103
	v_add_u32_e32 v130, s3, v119
	v_lshlrev_b64 v[102:103], 5, v[130:131]
	v_lshl_add_u64 v[102:103], v[0:1], 0, v[102:103]
	global_store_dwordx4 v[102:103], v[98:101], off
	s_waitcnt lgkmcnt(0)
	v_cndmask_b32_e64 v102, v104, v108, s[0:1]
	v_cndmask_b32_e32 v66, v82, v66, vcc
	v_cndmask_b32_e64 v100, v105, v107, s[0:1]
	v_xor_b32_e32 v82, 0x5000, v141
	v_cndmask_b32_e64 v98, v108, v110, s[0:1]
	v_cndmask_b32_e64 v103, v120, v102, s[0:1]
	v_cndmask_b32_e64 v101, v121, v100, s[0:1]
	v_or_b32_e32 v110, v140, v82
	v_cndmask_b32_e64 v99, v107, v106, s[0:1]
	v_bfi_b32 v101, s2, v100, v101
	v_bfi_b32 v100, s2, v103, v102
	ds_read2st64_b32 v[102:103], v110 offset1:1
	ds_read2st64_b32 v[104:105], v110 offset0:4 offset1:5
	ds_read2st64_b32 v[106:107], v110 offset0:6 offset1:7
	ds_read2st64_b32 v[108:109], v110 offset0:2 offset1:3
	v_cndmask_b32_e32 v67, v83, v67, vcc
	v_cndmask_b32_e32 v70, v86, v70, vcc
	s_waitcnt lgkmcnt(3)
	v_add_f32_e32 v66, v66, v102
	v_cndmask_b32_e32 v71, v87, v71, vcc
	v_add_f32_e32 v67, v67, v103
	v_cndmask_b32_e32 v68, v84, v68, vcc
	v_cndmask_b32_e32 v72, v88, v72, vcc
	v_cndmask_b32_e32 v69, v85, v69, vcc
	v_cndmask_b32_e32 v73, v89, v73, vcc
	s_waitcnt lgkmcnt(2)
	v_add_f32_e32 v70, v70, v104
	v_add_f32_e32 v71, v71, v105
	s_waitcnt lgkmcnt(0)
	v_add_f32_e32 v68, v68, v108
	v_add_f32_e32 v72, v72, v106
	v_add_f32_e32 v69, v69, v109
	v_cvt_pk_f16_f32 v82, v66, v67
	v_add_f32_e32 v66, v73, v107
	v_cvt_pk_f16_f32 v68, v68, v69
	v_cvt_pk_f16_f32 v69, v70, v71
	v_cvt_pk_f16_f32 v70, v72, v66
	v_cndmask_b32_e64 v66, v68, v70, s[0:1]
	v_cndmask_b32_e64 v67, v82, v69, s[0:1]
	ds_bpermute_b32 v71, v144, v66
	ds_bpermute_b32 v72, v144, v67
	v_lshl_add_u32 v118, v143, 7, v133
	v_add_u32_e32 v130, s4, v118
	v_lshlrev_b64 v[66:67], 5, v[130:131]
	v_lshl_add_u64 v[66:67], v[0:1], 0, v[66:67]
	global_store_dwordx4 v[66:67], v[98:101], off
	s_waitcnt lgkmcnt(1)
	v_cndmask_b32_e64 v67, v71, v68, s[0:1]
	v_cndmask_b32_e64 v68, v70, v71, s[0:1]
	s_waitcnt lgkmcnt(0)
	v_cndmask_b32_e64 v70, v69, v72, s[0:1]
	v_cndmask_b32_e64 v71, v120, v70, s[0:1]
	v_cndmask_b32_e64 v69, v121, v68, s[0:1]
	v_cndmask_b32_e64 v66, v72, v82, s[0:1]
	v_bfi_b32 v69, s2, v68, v69
	v_bfi_b32 v68, s2, v71, v70
	ds_read2st64_b32 v[70:71], v110 offset0:8 offset1:9
	ds_read2st64_b32 v[72:73], v110 offset0:12 offset1:13
	ds_read2st64_b32 v[82:83], v110 offset0:14 offset1:15
	ds_read2st64_b32 v[84:85], v110 offset0:10 offset1:11
	v_cndmask_b32_e32 v74, v90, v74, vcc
	v_cndmask_b32_e32 v78, v94, v78, vcc
	s_waitcnt lgkmcnt(3)
	v_add_f32_e32 v70, v74, v70
	v_cndmask_b32_e32 v74, v91, v75, vcc
	v_cndmask_b32_e32 v75, v95, v79, vcc
	v_add_f32_e32 v71, v74, v71
	s_waitcnt lgkmcnt(2)
	v_add_f32_e32 v73, v75, v73
	v_cndmask_b32_e32 v74, v92, v76, vcc
	v_cndmask_b32_e32 v75, v96, v80, vcc
	v_cndmask_b32_e32 v76, v93, v77, vcc
	v_cndmask_b32_e32 v77, v97, v81, vcc
	v_add_f32_e32 v72, v78, v72
	s_waitcnt lgkmcnt(0)
	v_add_f32_e32 v74, v74, v84
	v_add_f32_e32 v75, v75, v82
	v_add_f32_e32 v76, v76, v85
	v_cvt_pk_f16_f32 v78, v70, v71
	v_add_f32_e32 v70, v77, v83
	v_cvt_pk_f16_f32 v74, v74, v76
	v_cvt_pk_f16_f32 v72, v72, v73
	v_cvt_pk_f16_f32 v73, v75, v70
	v_cndmask_b32_e64 v70, v74, v73, s[0:1]
	v_cndmask_b32_e64 v71, v78, v72, s[0:1]
	ds_bpermute_b32 v75, v144, v70
	ds_bpermute_b32 v76, v144, v71
	v_add_u32_e32 v130, s5, v119
	v_lshlrev_b64 v[70:71], 5, v[130:131]
	v_lshl_add_u64 v[70:71], v[0:1], 0, v[70:71]
	global_store_dwordx4 v[70:71], v[66:69], off
	s_waitcnt lgkmcnt(0)
	v_cndmask_b32_e64 v70, v72, v76, s[0:1]
	v_cndmask_b32_e64 v71, v120, v70, s[0:1]
	v_cndmask_b32_e64 v68, v73, v75, s[0:1]
	v_cndmask_b32_e64 v69, v121, v68, s[0:1]
	v_add_u32_e32 v130, s6, v118
	v_bfi_b32 v69, s2, v68, v69
	v_bfi_b32 v68, s2, v71, v70
	v_lshlrev_b64 v[70:71], 5, v[130:131]
	v_cndmask_b32_e64 v67, v75, v74, s[0:1]
	v_cndmask_b32_e64 v66, v76, v78, s[0:1]
	v_lshl_add_u64 v[70:71], v[0:1], 0, v[70:71]
	v_cndmask_b32_e32 v34, v50, v34, vcc
	v_xor_b32_e32 v50, 0x6000, v141
	global_store_dwordx4 v[70:71], v[66:69], off
	v_or_b32_e32 v74, v140, v50
	ds_read2st64_b32 v[66:67], v74 offset1:1
	ds_read2st64_b32 v[68:69], v74 offset0:4 offset1:5
	ds_read2st64_b32 v[70:71], v74 offset0:6 offset1:7
	ds_read2st64_b32 v[72:73], v74 offset0:2 offset1:3
	v_cndmask_b32_e32 v35, v51, v35, vcc
	v_cndmask_b32_e32 v36, v52, v36, vcc
	v_cndmask_b32_e32 v37, v53, v37, vcc
	v_cndmask_b32_e32 v38, v54, v38, vcc
	s_waitcnt lgkmcnt(3)
	v_add_f32_e32 v34, v34, v66
	v_cndmask_b32_e32 v39, v55, v39, vcc
	v_add_f32_e32 v35, v35, v67
	v_cndmask_b32_e32 v40, v56, v40, vcc
	s_waitcnt lgkmcnt(0)
	v_add_f32_e32 v36, v36, v72
	v_cndmask_b32_e32 v41, v57, v41, vcc
	v_add_f32_e32 v37, v37, v73
	v_add_f32_e32 v38, v38, v68
	v_add_f32_e32 v39, v39, v69
	v_add_f32_e32 v40, v40, v70
	v_cvt_pk_f16_f32 v34, v34, v35
	v_cvt_pk_f16_f32 v35, v36, v37
	v_add_f32_e32 v36, v41, v71
	v_cvt_pk_f16_f32 v37, v38, v39
	v_cvt_pk_f16_f32 v36, v40, v36
	v_cndmask_b32_e64 v38, v35, v36, s[0:1]
	v_cndmask_b32_e64 v39, v34, v37, s[0:1]
	ds_bpermute_b32 v38, v144, v38
	ds_bpermute_b32 v39, v144, v39
	v_or_b32_e32 v40, 1, v143
	v_lshl_add_u32 v54, v40, 7, v133
	v_or_b32_e32 v55, v40, v145
	s_waitcnt lgkmcnt(1)
	v_cndmask_b32_e64 v35, v38, v35, s[0:1]
	v_cndmask_b32_e64 v36, v36, v38, s[0:1]
	s_waitcnt lgkmcnt(0)
	v_cndmask_b32_e64 v38, v37, v39, s[0:1]
	v_cndmask_b32_e64 v34, v39, v34, s[0:1]
	v_cndmask_b32_e64 v39, v120, v38, s[0:1]
	v_cndmask_b32_e64 v37, v121, v36, s[0:1]
	v_bfi_b32 v37, s2, v36, v37
	v_bfi_b32 v36, s2, v39, v38
	ds_read2st64_b32 v[38:39], v74 offset0:8 offset1:9
	ds_read2st64_b32 v[40:41], v74 offset0:12 offset1:13
	ds_read2st64_b32 v[50:51], v74 offset0:14 offset1:15
	ds_read2st64_b32 v[52:53], v74 offset0:10 offset1:11
	v_cndmask_b32_e32 v42, v58, v42, vcc
	v_cndmask_b32_e32 v46, v62, v46, vcc
	s_waitcnt lgkmcnt(3)
	v_add_f32_e32 v38, v42, v38
	v_cndmask_b32_e32 v42, v59, v43, vcc
	v_cndmask_b32_e32 v43, v63, v47, vcc
	v_add_f32_e32 v39, v42, v39
	s_waitcnt lgkmcnt(2)
	v_add_f32_e32 v41, v43, v41
	v_cndmask_b32_e32 v42, v60, v44, vcc
	v_cndmask_b32_e32 v43, v64, v48, vcc
	v_cndmask_b32_e32 v44, v61, v45, vcc
	v_cndmask_b32_e32 v45, v65, v49, vcc
	v_add_f32_e32 v40, v46, v40
	s_waitcnt lgkmcnt(0)
	v_add_f32_e32 v42, v42, v52
	v_add_f32_e32 v43, v43, v50
	v_add_f32_e32 v44, v44, v53
	v_cvt_pk_f16_f32 v46, v38, v39
	v_add_f32_e32 v38, v45, v51
	v_cvt_pk_f16_f32 v42, v42, v44
	v_cvt_pk_f16_f32 v40, v40, v41
	v_cvt_pk_f16_f32 v41, v43, v38
	v_cndmask_b32_e64 v38, v42, v41, s[0:1]
	v_cndmask_b32_e64 v39, v46, v40, s[0:1]
	ds_bpermute_b32 v43, v144, v38
	ds_bpermute_b32 v44, v144, v39
	v_add_u32_e32 v130, s3, v55
	v_lshlrev_b64 v[38:39], 5, v[130:131]
	v_lshl_add_u64 v[38:39], v[0:1], 0, v[38:39]
	global_store_dwordx4 v[38:39], v[34:37], off
	s_waitcnt lgkmcnt(0)
	v_cndmask_b32_e64 v38, v40, v44, s[0:1]
	v_cndmask_b32_e32 v2, v18, v2, vcc
	v_cndmask_b32_e64 v36, v41, v43, s[0:1]
	v_xor_b32_e32 v18, 0x7000, v141
	v_cndmask_b32_e64 v39, v120, v38, s[0:1]
	v_cndmask_b32_e64 v37, v121, v36, s[0:1]
	v_or_b32_e32 v18, v140, v18
	v_cndmask_b32_e64 v35, v43, v42, s[0:1]
	v_cndmask_b32_e64 v34, v44, v46, s[0:1]
	v_bfi_b32 v37, s2, v36, v37
	v_bfi_b32 v36, s2, v39, v38
	ds_read2st64_b32 v[38:39], v18 offset1:1
	ds_read2st64_b32 v[40:41], v18 offset0:4 offset1:5
	ds_read2st64_b32 v[42:43], v18 offset0:6 offset1:7
	ds_read2st64_b32 v[44:45], v18 offset0:2 offset1:3
	v_cndmask_b32_e32 v3, v19, v3, vcc
	v_cndmask_b32_e32 v6, v22, v6, vcc
	s_waitcnt lgkmcnt(3)
	v_add_f32_e32 v2, v2, v38
	v_cndmask_b32_e32 v7, v23, v7, vcc
	v_add_f32_e32 v3, v3, v39
	v_cndmask_b32_e32 v4, v20, v4, vcc
	v_cndmask_b32_e32 v8, v24, v8, vcc
	v_cndmask_b32_e32 v5, v21, v5, vcc
	v_cndmask_b32_e32 v9, v25, v9, vcc
	s_waitcnt lgkmcnt(2)
	v_add_f32_e32 v6, v6, v40
	v_add_f32_e32 v7, v7, v41
	s_waitcnt lgkmcnt(0)
	v_add_f32_e32 v4, v4, v44
	v_add_f32_e32 v8, v8, v42
	v_add_f32_e32 v5, v5, v45
	v_cvt_pk_f16_f32 v19, v2, v3
	v_add_f32_e32 v2, v9, v43
	v_cvt_pk_f16_f32 v4, v4, v5
	v_cvt_pk_f16_f32 v5, v6, v7
	v_cvt_pk_f16_f32 v6, v8, v2
	v_cndmask_b32_e64 v2, v4, v6, s[0:1]
	v_cndmask_b32_e64 v3, v19, v5, s[0:1]
	ds_bpermute_b32 v7, v144, v2
	ds_bpermute_b32 v8, v144, v3
	v_add_u32_e32 v130, s4, v54
	v_lshlrev_b64 v[2:3], 5, v[130:131]
	v_lshl_add_u64 v[2:3], v[0:1], 0, v[2:3]
	global_store_dwordx4 v[2:3], v[34:37], off
	s_waitcnt lgkmcnt(1)
	v_cndmask_b32_e64 v3, v7, v4, s[0:1]
	v_cndmask_b32_e64 v4, v6, v7, s[0:1]
	s_waitcnt lgkmcnt(0)
	v_cndmask_b32_e64 v6, v5, v8, s[0:1]
	v_cndmask_b32_e64 v7, v120, v6, s[0:1]
	v_cndmask_b32_e64 v5, v121, v4, s[0:1]
	v_cndmask_b32_e64 v2, v8, v19, s[0:1]
	v_bfi_b32 v5, s2, v4, v5
	v_bfi_b32 v4, s2, v7, v6
	v_cndmask_b32_e32 v19, v26, v10, vcc
	v_cndmask_b32_e32 v20, v30, v14, vcc
	v_cndmask_b32_e32 v21, v27, v11, vcc
	v_cndmask_b32_e32 v22, v31, v15, vcc
	ds_read2st64_b32 v[6:7], v18 offset0:8 offset1:9
	ds_read2st64_b32 v[8:9], v18 offset0:12 offset1:13
	ds_read2st64_b32 v[10:11], v18 offset0:14 offset1:15
	ds_read2st64_b32 v[14:15], v18 offset0:10 offset1:11
	v_cndmask_b32_e32 v12, v28, v12, vcc
	v_cndmask_b32_e32 v16, v32, v16, vcc
	v_cndmask_b32_e32 v13, v29, v13, vcc
	v_cndmask_b32_e32 v17, v33, v17, vcc
	s_waitcnt lgkmcnt(3)
	v_add_f32_e32 v6, v19, v6
	v_add_f32_e32 v7, v21, v7
	s_waitcnt lgkmcnt(2)
	v_add_f32_e32 v8, v20, v8
	v_add_f32_e32 v9, v22, v9
	s_waitcnt lgkmcnt(1)
	v_add_f32_e32 v10, v16, v10
	s_waitcnt lgkmcnt(0)
	v_add_f32_e32 v12, v12, v14
	v_add_f32_e32 v13, v13, v15
	v_cvt_pk_f16_f32 v14, v6, v7
	v_add_f32_e32 v6, v17, v11
	v_cvt_pk_f16_f32 v12, v12, v13
	v_cvt_pk_f16_f32 v8, v8, v9
	v_cvt_pk_f16_f32 v9, v10, v6
	v_cndmask_b32_e64 v6, v12, v9, s[0:1]
	v_cndmask_b32_e64 v7, v14, v8, s[0:1]
	ds_bpermute_b32 v10, v144, v6
	ds_bpermute_b32 v11, v144, v7
	v_add_u32_e32 v130, s5, v55
	v_lshlrev_b64 v[6:7], 5, v[130:131]
	v_lshl_add_u64 v[6:7], v[0:1], 0, v[6:7]
	global_store_dwordx4 v[6:7], v[2:5], off
	s_waitcnt lgkmcnt(0)
	v_cndmask_b32_e64 v6, v8, v11, s[0:1]
	v_cndmask_b32_e64 v7, v120, v6, s[0:1]
	v_cndmask_b32_e64 v4, v9, v10, s[0:1]
	v_cndmask_b32_e64 v5, v121, v4, s[0:1]
	v_add_u32_e32 v130, s6, v54
	v_bfi_b32 v5, s2, v4, v5
	v_bfi_b32 v4, s2, v7, v6
	v_lshlrev_b64 v[6:7], 5, v[130:131]
	v_cndmask_b32_e64 v3, v10, v12, s[0:1]
	v_cndmask_b32_e64 v2, v11, v14, s[0:1]
	v_lshl_add_u64 v[0:1], v[0:1], 0, v[6:7]
	global_store_dwordx4 v[0:1], v[2:5], off
	s_endpgm
